# baseline (speedup 1.0000x reference)
.LBB2_132:
	s_load_dwordx8 s[4:11], s[0:1], 0x0
	s_load_dwordx2 s[12:13], s[0:1], 0x20
	s_load_dwordx2 s[34:35], s[0:1], 0x28
	s_lshr_b32 s24, s2, 0
	s_and_b32 s25, s2, 0
	s_mul_i32 s26, s25, 16
	s_add_u32 s27, s26, 16
	v_lshl_or_b32 v55, s24, 14, v0
	s_waitcnt lgkmcnt(0)
	s_mov_b32 s14, 0x61a80
	s_mov_b32 s15, 0xf4240
	s_mov_b32 s16, 0x155cc0
	v_mov_b32_e32 v34, s4
	v_mov_b32_e32 v37, s5
	v_mov_b32_e32 v35, s6
	v_mov_b32_e32 v38, s7
	v_mov_b32_e32 v36, s8
	v_mov_b32_e32 v39, s9
	v_mov_b32_e32 v43, 0
	v_mov_b32_e32 v47, 0
	v_mov_b32_e32 v49, 0x30d40
	v_mov_b32_e32 v50, 0xfff6d840
	v_mov_b32_e32 v48, 0x61a80
	v_mov_b32_e32 v51, 0x61a80
	v_mov_b32_e32 v52, 0xf4240
	v_mov_b32_e32 v53, 0x30d40
	v_mov_b32_e32 v54, 0x61a80
	v_cmp_gt_u32_e64 s[18:19], s14, v55
	v_cmp_gt_u32_e64 s[20:21], s15, v55
	v_cmp_gt_u32_e64 s[22:23], s16, v55
	s_nop 0
	v_cndmask_b32_e64 v44, v36, v35, s[20:21]
	v_cndmask_b32_e64 v44, v44, v34, s[18:19]
	v_cndmask_b32_e64 v45, v39, v38, s[20:21]
	v_cndmask_b32_e64 v45, v45, v37, s[18:19]
	v_cndmask_b32_e64 v42, v50, v49, s[20:21]
	v_cndmask_b32_e64 v42, v42, v48, s[18:19]
	v_add_u32_e32 v42, v42, v55
	v_cndmask_b32_e64 v42, 0, v42, s[22:23]
	v_lshl_add_u64 v[46:47], v[42:43], 2, v[44:45]
	global_load_dword v3, v[46:47], off
	v_cndmask_b32_e64 v42, v52, v51, s[20:21]
	v_cndmask_b32_e64 v42, v42, 0, s[18:19]
	v_sub_u32_e32 v42, v55, v42
	v_cndmask_b32_e64 v42, 0, v42, s[22:23]
	v_lshl_add_u64 v[46:47], v[42:43], 2, v[44:45]
	global_load_dword v2, v[46:47], off
	v_add_u32_e32 v40, 0x400, v55
	v_cmp_gt_u32_e64 s[18:19], s14, v40
	v_cmp_gt_u32_e64 s[20:21], s15, v40
	v_cmp_gt_u32_e64 s[22:23], s16, v40
	s_nop 0
	v_cndmask_b32_e64 v44, v36, v35, s[20:21]
	v_cndmask_b32_e64 v44, v44, v34, s[18:19]
	v_cndmask_b32_e64 v45, v39, v38, s[20:21]
	v_cndmask_b32_e64 v45, v45, v37, s[18:19]
	v_cndmask_b32_e64 v42, v50, v49, s[20:21]
	v_cndmask_b32_e64 v42, v42, v48, s[18:19]
	v_add_u32_e32 v42, v42, v40
	v_cndmask_b32_e64 v42, 0, v42, s[22:23]
	v_lshl_add_u64 v[46:47], v[42:43], 2, v[44:45]
	global_load_dword v5, v[46:47], off
	v_cndmask_b32_e64 v42, v52, v51, s[20:21]
	v_cndmask_b32_e64 v42, v42, 0, s[18:19]
	v_sub_u32_e32 v42, v40, v42
	v_cndmask_b32_e64 v42, 0, v42, s[22:23]
	v_lshl_add_u64 v[46:47], v[42:43], 2, v[44:45]
	global_load_dword v4, v[46:47], off
	v_add_u32_e32 v40, 0x800, v55
	v_cmp_gt_u32_e64 s[18:19], s14, v40
	v_cmp_gt_u32_e64 s[20:21], s15, v40
	v_cmp_gt_u32_e64 s[22:23], s16, v40
	s_nop 0
	v_cndmask_b32_e64 v44, v36, v35, s[20:21]
	v_cndmask_b32_e64 v44, v44, v34, s[18:19]
	v_cndmask_b32_e64 v45, v39, v38, s[20:21]
	v_cndmask_b32_e64 v45, v45, v37, s[18:19]
	v_cndmask_b32_e64 v42, v50, v49, s[20:21]
	v_cndmask_b32_e64 v42, v42, v48, s[18:19]
	v_add_u32_e32 v42, v42, v40
	v_cndmask_b32_e64 v42, 0, v42, s[22:23]
	v_lshl_add_u64 v[46:47], v[42:43], 2, v[44:45]
	global_load_dword v7, v[46:47], off
	v_cndmask_b32_e64 v42, v52, v51, s[20:21]
	v_cndmask_b32_e64 v42, v42, 0, s[18:19]
	v_sub_u32_e32 v42, v40, v42
	v_cndmask_b32_e64 v42, 0, v42, s[22:23]
	v_lshl_add_u64 v[46:47], v[42:43], 2, v[44:45]
	global_load_dword v6, v[46:47], off
	v_add_u32_e32 v40, 0xc00, v55
	v_cmp_gt_u32_e64 s[18:19], s14, v40
	v_cmp_gt_u32_e64 s[20:21], s15, v40
	v_cmp_gt_u32_e64 s[22:23], s16, v40
	s_nop 0
	v_cndmask_b32_e64 v44, v36, v35, s[20:21]
	v_cndmask_b32_e64 v44, v44, v34, s[18:19]
	v_cndmask_b32_e64 v45, v39, v38, s[20:21]
	v_cndmask_b32_e64 v45, v45, v37, s[18:19]
	v_cndmask_b32_e64 v42, v50, v49, s[20:21]
	v_cndmask_b32_e64 v42, v42, v48, s[18:19]
	v_add_u32_e32 v42, v42, v40
	v_cndmask_b32_e64 v42, 0, v42, s[22:23]
	v_lshl_add_u64 v[46:47], v[42:43], 2, v[44:45]
	global_load_dword v9, v[46:47], off
	v_cndmask_b32_e64 v42, v52, v51, s[20:21]
	v_cndmask_b32_e64 v42, v42, 0, s[18:19]
	v_sub_u32_e32 v42, v40, v42
	v_cndmask_b32_e64 v42, 0, v42, s[22:23]
	v_lshl_add_u64 v[46:47], v[42:43], 2, v[44:45]
	global_load_dword v8, v[46:47], off
	v_add_u32_e32 v40, 0x1000, v55
	v_cmp_gt_u32_e64 s[18:19], s14, v40
	v_cmp_gt_u32_e64 s[20:21], s15, v40
	v_cmp_gt_u32_e64 s[22:23], s16, v40
	s_nop 0
	v_cndmask_b32_e64 v44, v36, v35, s[20:21]
	v_cndmask_b32_e64 v44, v44, v34, s[18:19]
	v_cndmask_b32_e64 v45, v39, v38, s[20:21]
	v_cndmask_b32_e64 v45, v45, v37, s[18:19]
	v_cndmask_b32_e64 v42, v50, v49, s[20:21]
	v_cndmask_b32_e64 v42, v42, v48, s[18:19]
	v_add_u32_e32 v42, v42, v40
	v_cndmask_b32_e64 v42, 0, v42, s[22:23]
	v_lshl_add_u64 v[46:47], v[42:43], 2, v[44:45]
	global_load_dword v11, v[46:47], off
	v_cndmask_b32_e64 v42, v52, v51, s[20:21]
	v_cndmask_b32_e64 v42, v42, 0, s[18:19]
	v_sub_u32_e32 v42, v40, v42
	v_cndmask_b32_e64 v42, 0, v42, s[22:23]
	v_lshl_add_u64 v[46:47], v[42:43], 2, v[44:45]
	global_load_dword v10, v[46:47], off
	v_add_u32_e32 v40, 0x1400, v55
	v_cmp_gt_u32_e64 s[18:19], s14, v40
	v_cmp_gt_u32_e64 s[20:21], s15, v40
	v_cmp_gt_u32_e64 s[22:23], s16, v40
	s_nop 0
	v_cndmask_b32_e64 v44, v36, v35, s[20:21]
	v_cndmask_b32_e64 v44, v44, v34, s[18:19]
	v_cndmask_b32_e64 v45, v39, v38, s[20:21]
	v_cndmask_b32_e64 v45, v45, v37, s[18:19]
	v_cndmask_b32_e64 v42, v50, v49, s[20:21]
	v_cndmask_b32_e64 v42, v42, v48, s[18:19]
	v_add_u32_e32 v42, v42, v40
	v_cndmask_b32_e64 v42, 0, v42, s[22:23]
	v_lshl_add_u64 v[46:47], v[42:43], 2, v[44:45]
	global_load_dword v13, v[46:47], off
	v_cndmask_b32_e64 v42, v52, v51, s[20:21]
	v_cndmask_b32_e64 v42, v42, 0, s[18:19]
	v_sub_u32_e32 v42, v40, v42
	v_cndmask_b32_e64 v42, 0, v42, s[22:23]
	v_lshl_add_u64 v[46:47], v[42:43], 2, v[44:45]
	global_load_dword v12, v[46:47], off
	v_add_u32_e32 v40, 0x1800, v55
	v_cmp_gt_u32_e64 s[18:19], s14, v40
	v_cmp_gt_u32_e64 s[20:21], s15, v40
	v_cmp_gt_u32_e64 s[22:23], s16, v40
	s_nop 0
	v_cndmask_b32_e64 v44, v36, v35, s[20:21]
	v_cndmask_b32_e64 v44, v44, v34, s[18:19]
	v_cndmask_b32_e64 v45, v39, v38, s[20:21]
	v_cndmask_b32_e64 v45, v45, v37, s[18:19]
	v_cndmask_b32_e64 v42, v50, v49, s[20:21]
	v_cndmask_b32_e64 v42, v42, v48, s[18:19]
	v_add_u32_e32 v42, v42, v40
	v_cndmask_b32_e64 v42, 0, v42, s[22:23]
	v_lshl_add_u64 v[46:47], v[42:43], 2, v[44:45]
	global_load_dword v15, v[46:47], off
	v_cndmask_b32_e64 v42, v52, v51, s[20:21]
	v_cndmask_b32_e64 v42, v42, 0, s[18:19]
	v_sub_u32_e32 v42, v40, v42
	v_cndmask_b32_e64 v42, 0, v42, s[22:23]
	v_lshl_add_u64 v[46:47], v[42:43], 2, v[44:45]
	global_load_dword v14, v[46:47], off
	v_add_u32_e32 v40, 0x1c00, v55
	v_cmp_gt_u32_e64 s[18:19], s14, v40
	v_cmp_gt_u32_e64 s[20:21], s15, v40
	v_cmp_gt_u32_e64 s[22:23], s16, v40
	s_nop 0
	v_cndmask_b32_e64 v44, v36, v35, s[20:21]
	v_cndmask_b32_e64 v44, v44, v34, s[18:19]
	v_cndmask_b32_e64 v45, v39, v38, s[20:21]
	v_cndmask_b32_e64 v45, v45, v37, s[18:19]
	v_cndmask_b32_e64 v42, v50, v49, s[20:21]
	v_cndmask_b32_e64 v42, v42, v48, s[18:19]
	v_add_u32_e32 v42, v42, v40
	v_cndmask_b32_e64 v42, 0, v42, s[22:23]
	v_lshl_add_u64 v[46:47], v[42:43], 2, v[44:45]
	global_load_dword v17, v[46:47], off
	v_cndmask_b32_e64 v42, v52, v51, s[20:21]
	v_cndmask_b32_e64 v42, v42, 0, s[18:19]
	v_sub_u32_e32 v42, v40, v42
	v_cndmask_b32_e64 v42, 0, v42, s[22:23]
	v_lshl_add_u64 v[46:47], v[42:43], 2, v[44:45]
	global_load_dword v16, v[46:47], off
	v_add_u32_e32 v40, 0x2000, v55
	v_cmp_gt_u32_e64 s[18:19], s14, v40
	v_cmp_gt_u32_e64 s[20:21], s15, v40
	v_cmp_gt_u32_e64 s[22:23], s16, v40
	s_nop 0
	v_cndmask_b32_e64 v44, v36, v35, s[20:21]
	v_cndmask_b32_e64 v44, v44, v34, s[18:19]
	v_cndmask_b32_e64 v45, v39, v38, s[20:21]
	v_cndmask_b32_e64 v45, v45, v37, s[18:19]
	v_cndmask_b32_e64 v42, v50, v49, s[20:21]
	v_cndmask_b32_e64 v42, v42, v48, s[18:19]
	v_add_u32_e32 v42, v42, v40
	v_cndmask_b32_e64 v42, 0, v42, s[22:23]
	v_lshl_add_u64 v[46:47], v[42:43], 2, v[44:45]
	global_load_dword v19, v[46:47], off
	v_cndmask_b32_e64 v42, v52, v51, s[20:21]
	v_cndmask_b32_e64 v42, v42, 0, s[18:19]
	v_sub_u32_e32 v42, v40, v42
	v_cndmask_b32_e64 v42, 0, v42, s[22:23]
	v_lshl_add_u64 v[46:47], v[42:43], 2, v[44:45]
	global_load_dword v18, v[46:47], off
	v_add_u32_e32 v40, 0x2400, v55
	v_cmp_gt_u32_e64 s[18:19], s14, v40
	v_cmp_gt_u32_e64 s[20:21], s15, v40
	v_cmp_gt_u32_e64 s[22:23], s16, v40
	s_nop 0
	v_cndmask_b32_e64 v44, v36, v35, s[20:21]
	v_cndmask_b32_e64 v44, v44, v34, s[18:19]
	v_cndmask_b32_e64 v45, v39, v38, s[20:21]
	v_cndmask_b32_e64 v45, v45, v37, s[18:19]
	v_cndmask_b32_e64 v42, v50, v49, s[20:21]
	v_cndmask_b32_e64 v42, v42, v48, s[18:19]
	v_add_u32_e32 v42, v42, v40
	v_cndmask_b32_e64 v42, 0, v42, s[22:23]
	v_lshl_add_u64 v[46:47], v[42:43], 2, v[44:45]
	global_load_dword v21, v[46:47], off
	v_cndmask_b32_e64 v42, v52, v51, s[20:21]
	v_cndmask_b32_e64 v42, v42, 0, s[18:19]
	v_sub_u32_e32 v42, v40, v42
	v_cndmask_b32_e64 v42, 0, v42, s[22:23]
	v_lshl_add_u64 v[46:47], v[42:43], 2, v[44:45]
	global_load_dword v20, v[46:47], off
	v_add_u32_e32 v40, 0x2800, v55
	v_cmp_gt_u32_e64 s[18:19], s14, v40
	v_cmp_gt_u32_e64 s[20:21], s15, v40
	v_cmp_gt_u32_e64 s[22:23], s16, v40
	s_nop 0
	v_cndmask_b32_e64 v44, v36, v35, s[20:21]
	v_cndmask_b32_e64 v44, v44, v34, s[18:19]
	v_cndmask_b32_e64 v45, v39, v38, s[20:21]
	v_cndmask_b32_e64 v45, v45, v37, s[18:19]
	v_cndmask_b32_e64 v42, v50, v49, s[20:21]
	v_cndmask_b32_e64 v42, v42, v48, s[18:19]
	v_add_u32_e32 v42, v42, v40
	v_cndmask_b32_e64 v42, 0, v42, s[22:23]
	v_lshl_add_u64 v[46:47], v[42:43], 2, v[44:45]
	global_load_dword v23, v[46:47], off
	v_cndmask_b32_e64 v42, v52, v51, s[20:21]
	v_cndmask_b32_e64 v42, v42, 0, s[18:19]
	v_sub_u32_e32 v42, v40, v42
	v_cndmask_b32_e64 v42, 0, v42, s[22:23]
	v_lshl_add_u64 v[46:47], v[42:43], 2, v[44:45]
	global_load_dword v22, v[46:47], off
	v_add_u32_e32 v40, 0x2c00, v55
	v_cmp_gt_u32_e64 s[18:19], s14, v40
	v_cmp_gt_u32_e64 s[20:21], s15, v40
	v_cmp_gt_u32_e64 s[22:23], s16, v40
	s_nop 0
	v_cndmask_b32_e64 v44, v36, v35, s[20:21]
	v_cndmask_b32_e64 v44, v44, v34, s[18:19]
	v_cndmask_b32_e64 v45, v39, v38, s[20:21]
	v_cndmask_b32_e64 v45, v45, v37, s[18:19]
	v_cndmask_b32_e64 v42, v50, v49, s[20:21]
	v_cndmask_b32_e64 v42, v42, v48, s[18:19]
	v_add_u32_e32 v42, v42, v40
	v_cndmask_b32_e64 v42, 0, v42, s[22:23]
	v_lshl_add_u64 v[46:47], v[42:43], 2, v[44:45]
	global_load_dword v25, v[46:47], off
	v_cndmask_b32_e64 v42, v52, v51, s[20:21]
	v_cndmask_b32_e64 v42, v42, 0, s[18:19]
	v_sub_u32_e32 v42, v40, v42
	v_cndmask_b32_e64 v42, 0, v42, s[22:23]
	v_lshl_add_u64 v[46:47], v[42:43], 2, v[44:45]
	global_load_dword v24, v[46:47], off
	v_add_u32_e32 v40, 0x3000, v55
	v_cmp_gt_u32_e64 s[18:19], s14, v40
	v_cmp_gt_u32_e64 s[20:21], s15, v40
	v_cmp_gt_u32_e64 s[22:23], s16, v40
	s_nop 0
	v_cndmask_b32_e64 v44, v36, v35, s[20:21]
	v_cndmask_b32_e64 v44, v44, v34, s[18:19]
	v_cndmask_b32_e64 v45, v39, v38, s[20:21]
	v_cndmask_b32_e64 v45, v45, v37, s[18:19]
	v_cndmask_b32_e64 v42, v50, v49, s[20:21]
	v_cndmask_b32_e64 v42, v42, v48, s[18:19]
	v_add_u32_e32 v42, v42, v40
	v_cndmask_b32_e64 v42, 0, v42, s[22:23]
	v_lshl_add_u64 v[46:47], v[42:43], 2, v[44:45]
	global_load_dword v27, v[46:47], off
	v_cndmask_b32_e64 v42, v52, v51, s[20:21]
	v_cndmask_b32_e64 v42, v42, 0, s[18:19]
	v_sub_u32_e32 v42, v40, v42
	v_cndmask_b32_e64 v42, 0, v42, s[22:23]
	v_lshl_add_u64 v[46:47], v[42:43], 2, v[44:45]
	global_load_dword v26, v[46:47], off
	v_add_u32_e32 v40, 0x3400, v55
	v_cmp_gt_u32_e64 s[18:19], s14, v40
	v_cmp_gt_u32_e64 s[20:21], s15, v40
	v_cmp_gt_u32_e64 s[22:23], s16, v40
	s_nop 0
	v_cndmask_b32_e64 v44, v36, v35, s[20:21]
	v_cndmask_b32_e64 v44, v44, v34, s[18:19]
	v_cndmask_b32_e64 v45, v39, v38, s[20:21]
	v_cndmask_b32_e64 v45, v45, v37, s[18:19]
	v_cndmask_b32_e64 v42, v50, v49, s[20:21]
	v_cndmask_b32_e64 v42, v42, v48, s[18:19]
	v_add_u32_e32 v42, v42, v40
	v_cndmask_b32_e64 v42, 0, v42, s[22:23]
	v_lshl_add_u64 v[46:47], v[42:43], 2, v[44:45]
	global_load_dword v29, v[46:47], off
	v_cndmask_b32_e64 v42, v52, v51, s[20:21]
	v_cndmask_b32_e64 v42, v42, 0, s[18:19]
	v_sub_u32_e32 v42, v40, v42
	v_cndmask_b32_e64 v42, 0, v42, s[22:23]
	v_lshl_add_u64 v[46:47], v[42:43], 2, v[44:45]
	global_load_dword v28, v[46:47], off
	v_add_u32_e32 v40, 0x3800, v55
	v_cmp_gt_u32_e64 s[18:19], s14, v40
	v_cmp_gt_u32_e64 s[20:21], s15, v40
	v_cmp_gt_u32_e64 s[22:23], s16, v40
	s_nop 0
	v_cndmask_b32_e64 v44, v36, v35, s[20:21]
	v_cndmask_b32_e64 v44, v44, v34, s[18:19]
	v_cndmask_b32_e64 v45, v39, v38, s[20:21]
	v_cndmask_b32_e64 v45, v45, v37, s[18:19]
	v_cndmask_b32_e64 v42, v50, v49, s[20:21]
	v_cndmask_b32_e64 v42, v42, v48, s[18:19]
	v_add_u32_e32 v42, v42, v40
	v_cndmask_b32_e64 v42, 0, v42, s[22:23]
	v_lshl_add_u64 v[46:47], v[42:43], 2, v[44:45]
	global_load_dword v31, v[46:47], off
	v_cndmask_b32_e64 v42, v52, v51, s[20:21]
	v_cndmask_b32_e64 v42, v42, 0, s[18:19]
	v_sub_u32_e32 v42, v40, v42
	v_cndmask_b32_e64 v42, 0, v42, s[22:23]
	v_lshl_add_u64 v[46:47], v[42:43], 2, v[44:45]
	global_load_dword v30, v[46:47], off
	v_add_u32_e32 v40, 0x3c00, v55
	v_cmp_gt_u32_e64 s[18:19], s14, v40
	v_cmp_gt_u32_e64 s[20:21], s15, v40
	v_cmp_gt_u32_e64 s[22:23], s16, v40
	s_nop 0
	v_cndmask_b32_e64 v44, v36, v35, s[20:21]
	v_cndmask_b32_e64 v44, v44, v34, s[18:19]
	v_cndmask_b32_e64 v45, v39, v38, s[20:21]
	v_cndmask_b32_e64 v45, v45, v37, s[18:19]
	v_cndmask_b32_e64 v42, v50, v49, s[20:21]
	v_cndmask_b32_e64 v42, v42, v48, s[18:19]
	v_add_u32_e32 v42, v42, v40
	v_cndmask_b32_e64 v42, 0, v42, s[22:23]
	v_lshl_add_u64 v[46:47], v[42:43], 2, v[44:45]
	global_load_dword v33, v[46:47], off
	v_cndmask_b32_e64 v42, v52, v51, s[20:21]
	v_cndmask_b32_e64 v42, v42, 0, s[18:19]
	v_sub_u32_e32 v42, v40, v42
	v_cndmask_b32_e64 v42, 0, v42, s[22:23]
	v_lshl_add_u64 v[46:47], v[42:43], 2, v[44:45]
	global_load_dword v32, v[46:47], off
	v_mov_b32_e32 v34, 0
	v_mov_b32_e32 v35, 0
	v_mov_b32_e32 v36, 0
	v_mov_b32_e32 v37, 0
	v_mov_b32_e32 v38, 0
	v_mov_b32_e32 v39, 0
	v_mov_b32_e32 v40, 0
	v_mov_b32_e32 v41, 0
	s_movk_i32 s3, 0x112
	v_mov_b32_e32 v42, v0
	v_mov_b32_e32 v43, 0
	v_cmp_le_u32_e32 vcc, s3, v42
	v_subrev_u32_e32 v44, s3, v42
	s_nop 1
	v_cndmask_b32_e64 v45, 0, 1, vcc
	v_cndmask_b32_e32 v42, v42, v44, vcc
	v_add_u32_e32 v43, v43, v45
	v_cmp_le_u32_e32 vcc, s3, v42
	v_subrev_u32_e32 v44, s3, v42
	s_nop 1
	v_cndmask_b32_e64 v45, 0, 1, vcc
	v_cndmask_b32_e32 v42, v42, v44, vcc
	v_add_u32_e32 v43, v43, v45
	v_cmp_le_u32_e32 vcc, s3, v42
	v_subrev_u32_e32 v44, s3, v42
	s_nop 1
	v_cndmask_b32_e64 v45, 0, 1, vcc
	v_cndmask_b32_e32 v42, v42, v44, vcc
	v_add_u32_e32 v43, v43, v45
	v_mul_u32_u24_e32 v44, 29, v43
	v_sub_u32_e32 v46, s24, v44
	v_mul_u32_u24_e32 v44, 0x1120, v44
	v_lshl_add_u32 v47, v42, 4, v44
	v_cmp_gt_u32_e64 s[38:39], 2, v43
	s_nop 1
	v_cndmask_b32_e64 v48, 0, 1, s[38:39]
	v_cmp_gt_u32_e32 vcc, 3, v43
	s_and_saveexec_b64 s[36:37], vcc
	s_cbranch_execz .Lsc_nohist
	global_load_dwordx4 v[52:55], v47, s[10:11]
	v_add_u32_e32 v49, 0x1120, v47
	global_load_dwordx4 v[56:59], v49, s[10:11]
	v_add_u32_e32 v49, 0x2240, v47
	global_load_dwordx4 v[60:63], v49, s[10:11]
	v_add_u32_e32 v49, 0x3360, v47
	global_load_dwordx4 v[64:67], v49, s[10:11]
	v_add_u32_e32 v49, 0x4480, v47
	global_load_dwordx4 v[68:71], v49, s[10:11]
	v_add_u32_e32 v49, 0x55a0, v47
	global_load_dwordx4 v[72:75], v49, s[10:11]
	v_add_u32_e32 v49, 0x66c0, v47
	global_load_dwordx4 v[76:79], v49, s[10:11]
	v_add_u32_e32 v49, 0x77e0, v47
	global_load_dwordx4 v[80:83], v49, s[10:11]
	v_add_u32_e32 v49, 0x8900, v47
	global_load_dwordx4 v[84:87], v49, s[10:11]
	v_add_u32_e32 v49, 0x9a20, v47
	global_load_dwordx4 v[88:91], v49, s[10:11]
	v_add_u32_e32 v49, 0xab40, v47
	global_load_dwordx4 v[92:95], v49, s[10:11]
	v_add_u32_e32 v49, 0xbc60, v47
	global_load_dwordx4 v[96:99], v49, s[10:11]
	v_add_u32_e32 v49, 0xcd80, v47
	global_load_dwordx4 v[100:103], v49, s[10:11]
	v_add_u32_e32 v49, 0xdea0, v47
	global_load_dwordx4 v[104:107], v49, s[10:11]
	v_add_u32_e32 v49, 0xefc0, v47
	global_load_dwordx4 v[108:111], v49, s[10:11]
	v_add_u32_e32 v49, 0x100e0, v47
	global_load_dwordx4 v[112:115], v49, s[10:11]
	v_add_u32_e32 v49, 0x11200, v47
	global_load_dwordx4 v[116:119], v49, s[10:11]
	v_add_u32_e32 v49, 0x12320, v47
	global_load_dwordx4 v[120:123], v49, s[10:11]
	v_add_u32_e32 v49, 0x13440, v47
	global_load_dwordx4 v[124:127], v49, s[10:11]
	s_waitcnt vmcnt(18)
	v_cmp_lt_i32_e32 vcc, 0, v46
	s_nop 1
	v_cndmask_b32_e64 v50, 0, 1, vcc
	v_add_u32_e32 v34, v34, v52
	v_add_u32_e32 v35, v35, v53
	v_add_u32_e32 v36, v36, v54
	v_add_u32_e32 v37, v37, v55
	v_mad_u32_u24 v38, v52, v50, v38
	v_mad_u32_u24 v39, v53, v50, v39
	v_mad_u32_u24 v40, v54, v50, v40
	v_mad_u32_u24 v41, v55, v50, v41
	v_add_u32_e32 v49, 0x14560, v47
	global_load_dwordx4 v[52:55], v49, s[10:11]
	s_waitcnt vmcnt(18)
	v_cmp_lt_i32_e32 vcc, 1, v46
	s_nop 1
	v_cndmask_b32_e64 v50, 0, 1, vcc
	v_add_u32_e32 v34, v34, v56
	v_add_u32_e32 v35, v35, v57
	v_add_u32_e32 v36, v36, v58
	v_add_u32_e32 v37, v37, v59
	v_mad_u32_u24 v38, v56, v50, v38
	v_mad_u32_u24 v39, v57, v50, v39
	v_mad_u32_u24 v40, v58, v50, v40
	v_mad_u32_u24 v41, v59, v50, v41
	v_add_u32_e32 v49, 0x15680, v47
	global_load_dwordx4 v[56:59], v49, s[10:11]
	s_waitcnt vmcnt(18)
	v_cmp_lt_i32_e32 vcc, 2, v46
	s_nop 1
	v_cndmask_b32_e64 v50, 0, 1, vcc
	v_add_u32_e32 v34, v34, v60
	v_add_u32_e32 v35, v35, v61
	v_add_u32_e32 v36, v36, v62
	v_add_u32_e32 v37, v37, v63
	v_mad_u32_u24 v38, v60, v50, v38
	v_mad_u32_u24 v39, v61, v50, v39
	v_mad_u32_u24 v40, v62, v50, v40
	v_mad_u32_u24 v41, v63, v50, v41
	v_add_u32_e32 v49, 0x167a0, v47
	global_load_dwordx4 v[60:63], v49, s[10:11]
	s_waitcnt vmcnt(18)
	v_cmp_lt_i32_e32 vcc, 3, v46
	s_nop 1
	v_cndmask_b32_e64 v50, 0, 1, vcc
	v_add_u32_e32 v34, v34, v64
	v_add_u32_e32 v35, v35, v65
	v_add_u32_e32 v36, v36, v66
	v_add_u32_e32 v37, v37, v67
	v_mad_u32_u24 v38, v64, v50, v38
	v_mad_u32_u24 v39, v65, v50, v39
	v_mad_u32_u24 v40, v66, v50, v40
	v_mad_u32_u24 v41, v67, v50, v41
	v_add_u32_e32 v49, 0x178c0, v47
	global_load_dwordx4 v[64:67], v49, s[10:11]
	s_waitcnt vmcnt(18)
	v_cmp_lt_i32_e32 vcc, 4, v46
	s_nop 1
	v_cndmask_b32_e64 v50, 0, 1, vcc
	v_add_u32_e32 v34, v34, v68
	v_add_u32_e32 v35, v35, v69
	v_add_u32_e32 v36, v36, v70
	v_add_u32_e32 v37, v37, v71
	v_mad_u32_u24 v38, v68, v50, v38
	v_mad_u32_u24 v39, v69, v50, v39
	v_mad_u32_u24 v40, v70, v50, v40
	v_mad_u32_u24 v41, v71, v50, v41
	v_add_u32_e32 v49, 0x189e0, v47
	global_load_dwordx4 v[68:71], v49, s[10:11]
	s_waitcnt vmcnt(18)
	v_cmp_lt_i32_e32 vcc, 5, v46
	s_nop 1
	v_cndmask_b32_e64 v50, 0, 1, vcc
	v_add_u32_e32 v34, v34, v72
	v_add_u32_e32 v35, v35, v73
	v_add_u32_e32 v36, v36, v74
	v_add_u32_e32 v37, v37, v75
	v_mad_u32_u24 v38, v72, v50, v38
	v_mad_u32_u24 v39, v73, v50, v39
	v_mad_u32_u24 v40, v74, v50, v40
	v_mad_u32_u24 v41, v75, v50, v41
	v_add_u32_e32 v49, 0x19b00, v47
	global_load_dwordx4 v[72:75], v49, s[10:11]
	s_waitcnt vmcnt(18)
	v_cmp_lt_i32_e32 vcc, 6, v46
	s_nop 1
	v_cndmask_b32_e64 v50, 0, 1, vcc
	v_add_u32_e32 v34, v34, v76
	v_add_u32_e32 v35, v35, v77
	v_add_u32_e32 v36, v36, v78
	v_add_u32_e32 v37, v37, v79
	v_mad_u32_u24 v38, v76, v50, v38
	v_mad_u32_u24 v39, v77, v50, v39
	v_mad_u32_u24 v40, v78, v50, v40
	v_mad_u32_u24 v41, v79, v50, v41
	v_add_u32_e32 v49, 0x1ac20, v47
	global_load_dwordx4 v[76:79], v49, s[10:11]
	s_waitcnt vmcnt(18)
	v_cmp_lt_i32_e32 vcc, 7, v46
	s_nop 1
	v_cndmask_b32_e64 v50, 0, 1, vcc
	v_add_u32_e32 v34, v34, v80
	v_add_u32_e32 v35, v35, v81
	v_add_u32_e32 v36, v36, v82
	v_add_u32_e32 v37, v37, v83
	v_mad_u32_u24 v38, v80, v50, v38
	v_mad_u32_u24 v39, v81, v50, v39
	v_mad_u32_u24 v40, v82, v50, v40
	v_mad_u32_u24 v41, v83, v50, v41
	v_add_u32_e32 v49, 0x1bd40, v47
	global_load_dwordx4 v[80:83], v49, s[10:11]
	s_waitcnt vmcnt(18)
	v_cmp_lt_i32_e32 vcc, 8, v46
	s_nop 1
	v_cndmask_b32_e64 v50, 0, 1, vcc
	v_add_u32_e32 v34, v34, v84
	v_add_u32_e32 v35, v35, v85
	v_add_u32_e32 v36, v36, v86
	v_add_u32_e32 v37, v37, v87
	v_mad_u32_u24 v38, v84, v50, v38
	v_mad_u32_u24 v39, v85, v50, v39
	v_mad_u32_u24 v40, v86, v50, v40
	v_mad_u32_u24 v41, v87, v50, v41
	v_add_u32_e32 v49, 0x1ce60, v47
	global_load_dwordx4 v[84:87], v49, s[10:11]
	s_waitcnt vmcnt(18)
	v_cmp_lt_i32_e32 vcc, 9, v46
	s_nop 1
	v_cndmask_b32_e64 v50, 0, 1, vcc
	v_add_u32_e32 v34, v34, v88
	v_add_u32_e32 v35, v35, v89
	v_add_u32_e32 v36, v36, v90
	v_add_u32_e32 v37, v37, v91
	v_mad_u32_u24 v38, v88, v50, v38
	v_mad_u32_u24 v39, v89, v50, v39
	v_mad_u32_u24 v40, v90, v50, v40
	v_mad_u32_u24 v41, v91, v50, v41
	v_add_u32_e32 v49, 0x1df80, v47
	global_load_dwordx4 v[88:91], v49, s[10:11]
	s_waitcnt vmcnt(18)
	v_cmp_lt_i32_e32 vcc, 10, v46
	s_nop 1
	v_cndmask_b32_e64 v50, 0, 1, vcc
	v_add_u32_e32 v34, v34, v92
	v_add_u32_e32 v35, v35, v93
	v_add_u32_e32 v36, v36, v94
	v_add_u32_e32 v37, v37, v95
	v_mad_u32_u24 v38, v92, v50, v38
	v_mad_u32_u24 v39, v93, v50, v39
	v_mad_u32_u24 v40, v94, v50, v40
	v_mad_u32_u24 v41, v95, v50, v41
	s_waitcnt vmcnt(17)
	v_cmp_lt_i32_e32 vcc, 11, v46
	s_nop 1
	v_cndmask_b32_e64 v50, 0, 1, vcc
	v_add_u32_e32 v34, v34, v96
	v_add_u32_e32 v35, v35, v97
	v_add_u32_e32 v36, v36, v98
	v_add_u32_e32 v37, v37, v99
	v_mad_u32_u24 v38, v96, v50, v38
	v_mad_u32_u24 v39, v97, v50, v39
	v_mad_u32_u24 v40, v98, v50, v40
	v_mad_u32_u24 v41, v99, v50, v41
	s_waitcnt vmcnt(16)
	v_cmp_lt_i32_e32 vcc, 12, v46
	s_nop 1
	v_cndmask_b32_e64 v50, 0, 1, vcc
	v_add_u32_e32 v34, v34, v100
	v_add_u32_e32 v35, v35, v101
	v_add_u32_e32 v36, v36, v102
	v_add_u32_e32 v37, v37, v103
	v_mad_u32_u24 v38, v100, v50, v38
	v_mad_u32_u24 v39, v101, v50, v39
	v_mad_u32_u24 v40, v102, v50, v40
	v_mad_u32_u24 v41, v103, v50, v41
	s_waitcnt vmcnt(15)
	v_cmp_lt_i32_e32 vcc, 13, v46
	s_nop 1
	v_cndmask_b32_e64 v50, 0, 1, vcc
	v_add_u32_e32 v34, v34, v104
	v_add_u32_e32 v35, v35, v105
	v_add_u32_e32 v36, v36, v106
	v_add_u32_e32 v37, v37, v107
	v_mad_u32_u24 v38, v104, v50, v38
	v_mad_u32_u24 v39, v105, v50, v39
	v_mad_u32_u24 v40, v106, v50, v40
	v_mad_u32_u24 v41, v107, v50, v41
	s_waitcnt vmcnt(14)
	v_cmp_lt_i32_e32 vcc, 14, v46
	s_nop 1
	v_cndmask_b32_e64 v50, 0, 1, vcc
	v_add_u32_e32 v34, v34, v108
	v_add_u32_e32 v35, v35, v109
	v_add_u32_e32 v36, v36, v110
	v_add_u32_e32 v37, v37, v111
	v_mad_u32_u24 v38, v108, v50, v38
	v_mad_u32_u24 v39, v109, v50, v39
	v_mad_u32_u24 v40, v110, v50, v40
	v_mad_u32_u24 v41, v111, v50, v41
	s_waitcnt vmcnt(13)
	v_cmp_lt_i32_e32 vcc, 15, v46
	s_nop 1
	v_cndmask_b32_e64 v50, 0, 1, vcc
	v_add_u32_e32 v34, v34, v112
	v_add_u32_e32 v35, v35, v113
	v_add_u32_e32 v36, v36, v114
	v_add_u32_e32 v37, v37, v115
	v_mad_u32_u24 v38, v112, v50, v38
	v_mad_u32_u24 v39, v113, v50, v39
	v_mad_u32_u24 v40, v114, v50, v40
	v_mad_u32_u24 v41, v115, v50, v41
	s_waitcnt vmcnt(12)
	v_cmp_lt_i32_e32 vcc, 16, v46
	s_nop 1
	v_cndmask_b32_e64 v50, 0, 1, vcc
	v_add_u32_e32 v34, v34, v116
	v_add_u32_e32 v35, v35, v117
	v_add_u32_e32 v36, v36, v118
	v_add_u32_e32 v37, v37, v119
	v_mad_u32_u24 v38, v116, v50, v38
	v_mad_u32_u24 v39, v117, v50, v39
	v_mad_u32_u24 v40, v118, v50, v40
	v_mad_u32_u24 v41, v119, v50, v41
	s_waitcnt vmcnt(11)
	v_cmp_lt_i32_e32 vcc, 17, v46
	s_nop 1
	v_cndmask_b32_e64 v50, 0, 1, vcc
	v_add_u32_e32 v34, v34, v120
	v_add_u32_e32 v35, v35, v121
	v_add_u32_e32 v36, v36, v122
	v_add_u32_e32 v37, v37, v123
	v_mad_u32_u24 v38, v120, v50, v38
	v_mad_u32_u24 v39, v121, v50, v39
	v_mad_u32_u24 v40, v122, v50, v40
	v_mad_u32_u24 v41, v123, v50, v41
	s_waitcnt vmcnt(10)
	v_cmp_lt_i32_e32 vcc, 18, v46
	s_nop 1
	v_cndmask_b32_e64 v50, 0, 1, vcc
	v_add_u32_e32 v34, v34, v124
	v_add_u32_e32 v35, v35, v125
	v_add_u32_e32 v36, v36, v126
	v_add_u32_e32 v37, v37, v127
	v_mad_u32_u24 v38, v124, v50, v38
	v_mad_u32_u24 v39, v125, v50, v39
	v_mad_u32_u24 v40, v126, v50, v40
	v_mad_u32_u24 v41, v127, v50, v41
	s_waitcnt vmcnt(9)
	v_cmp_lt_i32_e32 vcc, 19, v46
	s_nop 1
	v_cndmask_b32_e64 v50, 0, 1, vcc
	v_add_u32_e32 v34, v34, v52
	v_add_u32_e32 v35, v35, v53
	v_add_u32_e32 v36, v36, v54
	v_add_u32_e32 v37, v37, v55
	v_mad_u32_u24 v38, v52, v50, v38
	v_mad_u32_u24 v39, v53, v50, v39
	v_mad_u32_u24 v40, v54, v50, v40
	v_mad_u32_u24 v41, v55, v50, v41
	s_waitcnt vmcnt(8)
	v_cmp_lt_i32_e32 vcc, 20, v46
	s_nop 1
	v_cndmask_b32_e64 v50, 0, 1, vcc
	v_add_u32_e32 v34, v34, v56
	v_add_u32_e32 v35, v35, v57
	v_add_u32_e32 v36, v36, v58
	v_add_u32_e32 v37, v37, v59
	v_mad_u32_u24 v38, v56, v50, v38
	v_mad_u32_u24 v39, v57, v50, v39
	v_mad_u32_u24 v40, v58, v50, v40
	v_mad_u32_u24 v41, v59, v50, v41
	s_waitcnt vmcnt(7)
	v_cmp_lt_i32_e32 vcc, 21, v46
	s_nop 1
	v_cndmask_b32_e64 v50, 0, 1, vcc
	v_add_u32_e32 v34, v34, v60
	v_add_u32_e32 v35, v35, v61
	v_add_u32_e32 v36, v36, v62
	v_add_u32_e32 v37, v37, v63
	v_mad_u32_u24 v38, v60, v50, v38
	v_mad_u32_u24 v39, v61, v50, v39
	v_mad_u32_u24 v40, v62, v50, v40
	v_mad_u32_u24 v41, v63, v50, v41
	s_waitcnt vmcnt(6)
	v_cmp_lt_i32_e32 vcc, 22, v46
	s_nop 1
	v_cndmask_b32_e64 v50, 0, 1, vcc
	v_add_u32_e32 v34, v34, v64
	v_add_u32_e32 v35, v35, v65
	v_add_u32_e32 v36, v36, v66
	v_add_u32_e32 v37, v37, v67
	v_mad_u32_u24 v38, v64, v50, v38
	v_mad_u32_u24 v39, v65, v50, v39
	v_mad_u32_u24 v40, v66, v50, v40
	v_mad_u32_u24 v41, v67, v50, v41
	s_waitcnt vmcnt(5)
	v_cmp_lt_i32_e32 vcc, 23, v46
	s_nop 1
	v_cndmask_b32_e64 v50, 0, 1, vcc
	v_add_u32_e32 v34, v34, v68
	v_add_u32_e32 v35, v35, v69
	v_add_u32_e32 v36, v36, v70
	v_add_u32_e32 v37, v37, v71
	v_mad_u32_u24 v38, v68, v50, v38
	v_mad_u32_u24 v39, v69, v50, v39
	v_mad_u32_u24 v40, v70, v50, v40
	v_mad_u32_u24 v41, v71, v50, v41
	s_waitcnt vmcnt(4)
	v_cmp_lt_i32_e32 vcc, 24, v46
	s_nop 1
	v_cndmask_b32_e64 v50, 0, 1, vcc
	v_add_u32_e32 v34, v34, v72
	v_add_u32_e32 v35, v35, v73
	v_add_u32_e32 v36, v36, v74
	v_add_u32_e32 v37, v37, v75
	v_mad_u32_u24 v38, v72, v50, v38
	v_mad_u32_u24 v39, v73, v50, v39
	v_mad_u32_u24 v40, v74, v50, v40
	v_mad_u32_u24 v41, v75, v50, v41
	s_waitcnt vmcnt(3)
	v_cmp_lt_i32_e32 vcc, 25, v46
	s_nop 1
	v_cndmask_b32_e64 v50, 0, 1, vcc
	v_add_u32_e32 v34, v34, v76
	v_add_u32_e32 v35, v35, v77
	v_add_u32_e32 v36, v36, v78
	v_add_u32_e32 v37, v37, v79
	v_mad_u32_u24 v38, v76, v50, v38
	v_mad_u32_u24 v39, v77, v50, v39
	v_mad_u32_u24 v40, v78, v50, v40
	v_mad_u32_u24 v41, v79, v50, v41
	s_waitcnt vmcnt(2)
	v_cmp_lt_i32_e32 vcc, 26, v46
	s_nop 1
	v_cndmask_b32_e64 v50, 0, 1, vcc
	v_add_u32_e32 v34, v34, v80
	v_add_u32_e32 v35, v35, v81
	v_add_u32_e32 v36, v36, v82
	v_add_u32_e32 v37, v37, v83
	v_mad_u32_u24 v38, v80, v50, v38
	v_mad_u32_u24 v39, v81, v50, v39
	v_mad_u32_u24 v40, v82, v50, v40
	v_mad_u32_u24 v41, v83, v50, v41
	s_waitcnt vmcnt(1)
	v_cmp_lt_i32_e32 vcc, 27, v46
	s_nop 1
	v_cndmask_b32_e64 v50, 0, 1, vcc
	v_add_u32_e32 v34, v34, v84
	v_add_u32_e32 v35, v35, v85
	v_add_u32_e32 v36, v36, v86
	v_add_u32_e32 v37, v37, v87
	v_mad_u32_u24 v38, v84, v50, v38
	v_mad_u32_u24 v39, v85, v50, v39
	v_mad_u32_u24 v40, v86, v50, v40
	v_mad_u32_u24 v41, v87, v50, v41
	s_waitcnt vmcnt(0)
	v_cmp_lt_i32_e32 vcc, 28, v46
	s_nop 1
	v_cndmask_b32_e64 v50, 0, 1, vcc
	v_mad_u32_u24 v34, v88, v48, v34
	v_mad_u32_u24 v35, v89, v48, v35
	v_mad_u32_u24 v36, v90, v48, v36
	v_mad_u32_u24 v37, v91, v48, v37
	v_mad_u32_u24 v38, v88, v50, v38
	v_mad_u32_u24 v39, v89, v50, v39
	v_mad_u32_u24 v40, v90, v50, v40
	v_mad_u32_u24 v41, v91, v50, v41
	v_mul_u32_u24_e32 v44, 0x2240, v43
	v_lshl_add_u32 v44, v42, 4, v44
	ds_write_b128 v44, v[34:37] offset:14336
	ds_write_b128 v44, v[38:41] offset:18720
.Lsc_nohist:
	s_mov_b64 exec, s[36:37]
	s_waitcnt lgkmcnt(0)
	s_barrier
	v_mov_b32_e32 v34, 0
	v_mov_b32_e32 v35, 0
	v_mov_b32_e32 v36, 0
	v_mov_b32_e32 v37, 0
	v_lshlrev_b32_e32 v38, 3, v0
	v_cmp_gt_u32_e32 vcc, 0x224, v0
	s_and_saveexec_b64 s[36:37], vcc
	ds_read_b64 v[40:41], v38 offset:14336
	ds_read_b64 v[42:43], v38 offset:18720
	ds_read_b64 v[44:45], v38 offset:23104
	ds_read_b64 v[46:47], v38 offset:27488
	ds_read_b64 v[48:49], v38 offset:31872
	ds_read_b64 v[50:51], v38 offset:36256
	s_waitcnt lgkmcnt(0)
	v_add3_u32 v34, v40, v44, v48
	v_add3_u32 v35, v41, v45, v49
	v_add3_u32 v36, v42, v46, v50
	v_add3_u32 v37, v43, v47, v51
	s_mov_b64 exec, s[36:37]
	s_waitcnt vmcnt(0)
	v_mov_b32_e32 v53, 0x30d40
	v_mov_b32_e32 v54, 0x61a80
	v_lshl_or_b32 v55, s24, 14, v0
	v_mov_b32_e32 v44, -1
	v_cmp_gt_u32_e64 s[18:19], s14, v55
	v_cmp_gt_u32_e64 s[20:21], s15, v55
	v_cmp_gt_u32_e64 s[22:23], s16, v55
	s_nop 0
	v_cndmask_b32_e64 v42, v54, v53, s[20:21]
	v_cndmask_b32_e64 v42, v42, 0, s[18:19]
	v_add_u32_e32 v3, v3, v42
	v_cndmask_b32_e64 v3, v44, v3, s[22:23]
	v_cndmask_b32_e64 v2, 0, v2, s[22:23]
	v_add_u32_e32 v40, 0x400, v55
	v_cmp_gt_u32_e64 s[18:19], s14, v40
	v_cmp_gt_u32_e64 s[20:21], s15, v40
	v_cmp_gt_u32_e64 s[22:23], s16, v40
	s_nop 0
	v_cndmask_b32_e64 v42, v54, v53, s[20:21]
	v_cndmask_b32_e64 v42, v42, 0, s[18:19]
	v_add_u32_e32 v5, v5, v42
	v_cndmask_b32_e64 v5, v44, v5, s[22:23]
	v_cndmask_b32_e64 v4, 0, v4, s[22:23]
	v_add_u32_e32 v40, 0x800, v55
	v_cmp_gt_u32_e64 s[18:19], s14, v40
	v_cmp_gt_u32_e64 s[20:21], s15, v40
	v_cmp_gt_u32_e64 s[22:23], s16, v40
	s_nop 0
	v_cndmask_b32_e64 v42, v54, v53, s[20:21]
	v_cndmask_b32_e64 v42, v42, 0, s[18:19]
	v_add_u32_e32 v7, v7, v42
	v_cndmask_b32_e64 v7, v44, v7, s[22:23]
	v_cndmask_b32_e64 v6, 0, v6, s[22:23]
	v_add_u32_e32 v40, 0xc00, v55
	v_cmp_gt_u32_e64 s[18:19], s14, v40
	v_cmp_gt_u32_e64 s[20:21], s15, v40
	v_cmp_gt_u32_e64 s[22:23], s16, v40
	s_nop 0
	v_cndmask_b32_e64 v42, v54, v53, s[20:21]
	v_cndmask_b32_e64 v42, v42, 0, s[18:19]
	v_add_u32_e32 v9, v9, v42
	v_cndmask_b32_e64 v9, v44, v9, s[22:23]
	v_cndmask_b32_e64 v8, 0, v8, s[22:23]
	v_add_u32_e32 v40, 0x1000, v55
	v_cmp_gt_u32_e64 s[18:19], s14, v40
	v_cmp_gt_u32_e64 s[20:21], s15, v40
	v_cmp_gt_u32_e64 s[22:23], s16, v40
	s_nop 0
	v_cndmask_b32_e64 v42, v54, v53, s[20:21]
	v_cndmask_b32_e64 v42, v42, 0, s[18:19]
	v_add_u32_e32 v11, v11, v42
	v_cndmask_b32_e64 v11, v44, v11, s[22:23]
	v_cndmask_b32_e64 v10, 0, v10, s[22:23]
	v_add_u32_e32 v40, 0x1400, v55
	v_cmp_gt_u32_e64 s[18:19], s14, v40
	v_cmp_gt_u32_e64 s[20:21], s15, v40
	v_cmp_gt_u32_e64 s[22:23], s16, v40
	s_nop 0
	v_cndmask_b32_e64 v42, v54, v53, s[20:21]
	v_cndmask_b32_e64 v42, v42, 0, s[18:19]
	v_add_u32_e32 v13, v13, v42
	v_cndmask_b32_e64 v13, v44, v13, s[22:23]
	v_cndmask_b32_e64 v12, 0, v12, s[22:23]
	v_add_u32_e32 v40, 0x1800, v55
	v_cmp_gt_u32_e64 s[18:19], s14, v40
	v_cmp_gt_u32_e64 s[20:21], s15, v40
	v_cmp_gt_u32_e64 s[22:23], s16, v40
	s_nop 0
	v_cndmask_b32_e64 v42, v54, v53, s[20:21]
	v_cndmask_b32_e64 v42, v42, 0, s[18:19]
	v_add_u32_e32 v15, v15, v42
	v_cndmask_b32_e64 v15, v44, v15, s[22:23]
	v_cndmask_b32_e64 v14, 0, v14, s[22:23]
	v_add_u32_e32 v40, 0x1c00, v55
	v_cmp_gt_u32_e64 s[18:19], s14, v40
	v_cmp_gt_u32_e64 s[20:21], s15, v40
	v_cmp_gt_u32_e64 s[22:23], s16, v40
	s_nop 0
	v_cndmask_b32_e64 v42, v54, v53, s[20:21]
	v_cndmask_b32_e64 v42, v42, 0, s[18:19]
	v_add_u32_e32 v17, v17, v42
	v_cndmask_b32_e64 v17, v44, v17, s[22:23]
	v_cndmask_b32_e64 v16, 0, v16, s[22:23]
	v_add_u32_e32 v40, 0x2000, v55
	v_cmp_gt_u32_e64 s[18:19], s14, v40
	v_cmp_gt_u32_e64 s[20:21], s15, v40
	v_cmp_gt_u32_e64 s[22:23], s16, v40
	s_nop 0
	v_cndmask_b32_e64 v42, v54, v53, s[20:21]
	v_cndmask_b32_e64 v42, v42, 0, s[18:19]
	v_add_u32_e32 v19, v19, v42
	v_cndmask_b32_e64 v19, v44, v19, s[22:23]
	v_cndmask_b32_e64 v18, 0, v18, s[22:23]
	v_add_u32_e32 v40, 0x2400, v55
	v_cmp_gt_u32_e64 s[18:19], s14, v40
	v_cmp_gt_u32_e64 s[20:21], s15, v40
	v_cmp_gt_u32_e64 s[22:23], s16, v40
	s_nop 0
	v_cndmask_b32_e64 v42, v54, v53, s[20:21]
	v_cndmask_b32_e64 v42, v42, 0, s[18:19]
	v_add_u32_e32 v21, v21, v42
	v_cndmask_b32_e64 v21, v44, v21, s[22:23]
	v_cndmask_b32_e64 v20, 0, v20, s[22:23]
	v_add_u32_e32 v40, 0x2800, v55
	v_cmp_gt_u32_e64 s[18:19], s14, v40
	v_cmp_gt_u32_e64 s[20:21], s15, v40
	v_cmp_gt_u32_e64 s[22:23], s16, v40
	s_nop 0
	v_cndmask_b32_e64 v42, v54, v53, s[20:21]
	v_cndmask_b32_e64 v42, v42, 0, s[18:19]
	v_add_u32_e32 v23, v23, v42
	v_cndmask_b32_e64 v23, v44, v23, s[22:23]
	v_cndmask_b32_e64 v22, 0, v22, s[22:23]
	v_add_u32_e32 v40, 0x2c00, v55
	v_cmp_gt_u32_e64 s[18:19], s14, v40
	v_cmp_gt_u32_e64 s[20:21], s15, v40
	v_cmp_gt_u32_e64 s[22:23], s16, v40
	s_nop 0
	v_cndmask_b32_e64 v42, v54, v53, s[20:21]
	v_cndmask_b32_e64 v42, v42, 0, s[18:19]
	v_add_u32_e32 v25, v25, v42
	v_cndmask_b32_e64 v25, v44, v25, s[22:23]
	v_cndmask_b32_e64 v24, 0, v24, s[22:23]
	v_add_u32_e32 v40, 0x3000, v55
	v_cmp_gt_u32_e64 s[18:19], s14, v40
	v_cmp_gt_u32_e64 s[20:21], s15, v40
	v_cmp_gt_u32_e64 s[22:23], s16, v40
	s_nop 0
	v_cndmask_b32_e64 v42, v54, v53, s[20:21]
	v_cndmask_b32_e64 v42, v42, 0, s[18:19]
	v_add_u32_e32 v27, v27, v42
	v_cndmask_b32_e64 v27, v44, v27, s[22:23]
	v_cndmask_b32_e64 v26, 0, v26, s[22:23]
	v_add_u32_e32 v40, 0x3400, v55
	v_cmp_gt_u32_e64 s[18:19], s14, v40
	v_cmp_gt_u32_e64 s[20:21], s15, v40
	v_cmp_gt_u32_e64 s[22:23], s16, v40
	s_nop 0
	v_cndmask_b32_e64 v42, v54, v53, s[20:21]
	v_cndmask_b32_e64 v42, v42, 0, s[18:19]
	v_add_u32_e32 v29, v29, v42
	v_cndmask_b32_e64 v29, v44, v29, s[22:23]
	v_cndmask_b32_e64 v28, 0, v28, s[22:23]
	v_add_u32_e32 v40, 0x3800, v55
	v_cmp_gt_u32_e64 s[18:19], s14, v40
	v_cmp_gt_u32_e64 s[20:21], s15, v40
	v_cmp_gt_u32_e64 s[22:23], s16, v40
	s_nop 0
	v_cndmask_b32_e64 v42, v54, v53, s[20:21]
	v_cndmask_b32_e64 v42, v42, 0, s[18:19]
	v_add_u32_e32 v31, v31, v42
	v_cndmask_b32_e64 v31, v44, v31, s[22:23]
	v_cndmask_b32_e64 v30, 0, v30, s[22:23]
	v_add_u32_e32 v40, 0x3c00, v55
	v_cmp_gt_u32_e64 s[18:19], s14, v40
	v_cmp_gt_u32_e64 s[20:21], s15, v40
	v_cmp_gt_u32_e64 s[22:23], s16, v40
	s_nop 0
	v_cndmask_b32_e64 v42, v54, v53, s[20:21]
	v_cndmask_b32_e64 v42, v42, 0, s[18:19]
	v_add_u32_e32 v33, v33, v42
	v_cndmask_b32_e64 v33, v44, v33, s[22:23]
	v_cndmask_b32_e64 v32, 0, v32, s[22:23]
	v_add_u32_e32 v38, v34, v35
	v_mov_b32_e32 v39, v38
	s_nop 1
	v_add_u32_dpp v39, v39, v39 row_shr:1 row_mask:0xf bank_mask:0xf bound_ctrl:0
	s_nop 1
	v_add_u32_dpp v39, v39, v39 row_shr:2 row_mask:0xf bank_mask:0xf bound_ctrl:0
	s_nop 1
	v_add_u32_dpp v39, v39, v39 row_shr:4 row_mask:0xf bank_mask:0xf bound_ctrl:0
	s_nop 1
	v_add_u32_dpp v39, v39, v39 row_shr:8 row_mask:0xf bank_mask:0xf bound_ctrl:0
	s_nop 1
	v_add_u32_dpp v39, v39, v39 row_bcast:15 row_mask:0xa bank_mask:0xf
	s_nop 1
	v_add_u32_dpp v39, v39, v39 row_bcast:31 row_mask:0xc bank_mask:0xf
	v_lshrrev_b32_e32 v40, 6, v0
	s_nop 0
	v_readfirstlane_b32 s3, v40
	v_readlane_b32 s14, v39, 63
	s_lshl_b32 s15, s3, 2
	s_add_u32 s15, s15, 0x2400
	v_mov_b32_e32 v41, s14
	v_mov_b32_e32 v42, s15
	s_mov_b64 s[38:39], exec
	s_mov_b64 exec, 1
	ds_write_b32 v42, v41
	s_mov_b64 exec, s[38:39]
	s_waitcnt lgkmcnt(0)
	s_barrier
	v_and_b32_e32 v41, 15, v0
	v_lshlrev_b32_e32 v41, 2, v41
	ds_read_b32 v41, v41 offset:9216
	s_waitcnt lgkmcnt(0)
	s_nop 1
	v_add_u32_dpp v41, v41, v41 row_shr:1 row_mask:0xf bank_mask:0xf bound_ctrl:0
	s_nop 1
	v_add_u32_dpp v41, v41, v41 row_shr:2 row_mask:0xf bank_mask:0xf bound_ctrl:0
	s_nop 1
	v_add_u32_dpp v41, v41, v41 row_shr:4 row_mask:0xf bank_mask:0xf bound_ctrl:0
	s_nop 1
	v_add_u32_dpp v41, v41, v41 row_shr:8 row_mask:0xf bank_mask:0xf bound_ctrl:0
	s_sub_u32 s15, s3, 1
	s_max_i32 s15, s15, 0
	s_nop 1
	v_readlane_b32 s16, v41, s15
	s_cmp_eq_u32 s3, 0
	s_cselect_b32 s16, 0, s16
	v_sub_u32_e32 v43, v39, v38
	v_add_u32_e32 v43, s16, v43
	v_add_u32_e32 v47, v43, v34
	v_add_u32_e32 v44, v43, v36
	v_add_u32_e32 v45, v47, v37
	v_mov_b32_e32 v46, v43
	v_mov_b32_e32 v48, 0
	v_mov_b32_e32 v49, 0
	v_lshlrev_b32_e32 v42, 3, v0
	v_cmp_gt_u32_e32 vcc, 0x224, v0
	s_and_saveexec_b64 s[36:37], vcc
	ds_write_b64 v42, v[44:45]
	ds_write_b64 v42, v[48:49] offset:4608
	s_cmp_lg_u32 s2, 0
	s_cbranch_scc1 .Lsc_nobb
	s_cbranch_execz .Lsc_nobb
	global_store_dwordx2 v42, v[46:47], s[12:13]

	.amdhsa_kernel _Z6k_prepPKiS0_S0_S0_PiP15HIP_vector_typeIiLj2EEPKfS6_S0_S0_S0_S6_S6_S6_PDF16_S7_6WSpecs
		.amdhsa_group_segment_fixed_size 145408
		.amdhsa_private_segment_fixed_size 0
		.amdhsa_kernarg_size 616
		.amdhsa_user_sgpr_count 2
		.amdhsa_user_sgpr_dispatch_ptr 0
		.amdhsa_user_sgpr_queue_ptr 0
		.amdhsa_user_sgpr_kernarg_segment_ptr 1
		.amdhsa_user_sgpr_dispatch_id 0
		.amdhsa_user_sgpr_kernarg_preload_length 0
		.amdhsa_user_sgpr_kernarg_preload_offset 0
		.amdhsa_user_sgpr_private_segment_size 0
		.amdhsa_uses_dynamic_stack 0
		.amdhsa_enable_private_segment 0
		.amdhsa_system_sgpr_workgroup_id_x 1
		.amdhsa_system_sgpr_workgroup_id_y 0
		.amdhsa_system_sgpr_workgroup_id_z 0
		.amdhsa_system_sgpr_workgroup_info 0
		.amdhsa_system_vgpr_workitem_id 0
		.amdhsa_next_free_vgpr 128
		.amdhsa_next_free_sgpr 40
		.amdhsa_accum_offset 128
		.amdhsa_reserve_vcc 1
		.amdhsa_float_round_mode_32 0
		.amdhsa_float_round_mode_16_64 0
		.amdhsa_float_denorm_mode_32 3
		.amdhsa_float_denorm_mode_16_64 3
		.amdhsa_dx10_clamp 1
		.amdhsa_ieee_mode 1
		.amdhsa_fp16_overflow 0
		.amdhsa_tg_split 0
		.amdhsa_exception_fp_ieee_invalid_op 0
		.amdhsa_exception_fp_denorm_src 0
		.amdhsa_exception_fp_ieee_div_zero 0
		.amdhsa_exception_fp_ieee_overflow 0
		.amdhsa_exception_fp_ieee_underflow 0
		.amdhsa_exception_fp_ieee_inexact 0
		.amdhsa_exception_int_div_zero 0
	.end_amdhsa_kernel

amdhsa.kernels:
  - .agpr_count:     0
    .args:
      - .actual_access:  read_only
        .address_space:  global
        .offset:         0
        .size:           8
        .value_kind:     global_buffer
      - .actual_access:  read_only
        .address_space:  global
        .offset:         8
        .size:           8
        .value_kind:     global_buffer
      - .actual_access:  write_only
        .address_space:  global
        .offset:         16
        .size:           8
        .value_kind:     global_buffer
      - .address_space:  global
        .offset:         24
        .size:           8
        .value_kind:     global_buffer
    .group_segment_fixed_size: 20736
    .kernarg_segment_align: 8
    .kernarg_segment_size: 32
    .language:       OpenCL C
    .language_version:
      - 2
      - 0
    .max_flat_workgroup_size: 256
    .name:           _Z6k_bcsrPK15HIP_vector_typeIiLj2EEPKiPiS5_
    .private_segment_fixed_size: 0
    .sgpr_count:     40
    .sgpr_spill_count: 0
    .symbol:         _Z6k_bcsrPK15HIP_vector_typeIiLj2EEPKiPiS5_.kd
    .uniform_work_group_size: 1
    .uses_dynamic_stack: false
    .vgpr_count:     64
    .vgpr_spill_count: 0
    .wavefront_size: 64
  - .agpr_count:     0
    .args:
      - .actual_access:  read_only
        .address_space:  global
        .offset:         0
        .size:           8
        .value_kind:     global_buffer
      - .actual_access:  read_only
        .address_space:  global
        .offset:         8
        .size:           8
        .value_kind:     global_buffer
      - .actual_access:  read_only
        .address_space:  global
        .offset:         16
        .size:           8
        .value_kind:     global_buffer
      - .actual_access:  write_only
        .address_space:  global
        .offset:         24
        .size:           8
        .value_kind:     global_buffer
      - .actual_access:  write_only
        .address_space:  global
        .offset:         32
        .size:           8
        .value_kind:     global_buffer
      - .actual_access:  read_only
        .address_space:  global
        .offset:         40
        .size:           8
        .value_kind:     global_buffer
      - .actual_access:  read_only
        .address_space:  global
        .offset:         48
        .size:           8
        .value_kind:     global_buffer
      - .actual_access:  read_only
        .address_space:  global
        .offset:         56
        .size:           8
        .value_kind:     global_buffer
      - .actual_access:  read_only
        .address_space:  global
        .offset:         64
        .size:           8
        .value_kind:     global_buffer
      - .actual_access:  read_only
        .address_space:  global
        .offset:         72
        .size:           8
        .value_kind:     global_buffer
      - .actual_access:  read_only
        .address_space:  global
        .offset:         80
        .size:           8
        .value_kind:     global_buffer
      - .actual_access:  read_only
        .address_space:  global
        .offset:         88
        .size:           8
        .value_kind:     global_buffer
      - .actual_access:  read_only
        .address_space:  global
        .offset:         96
        .size:           8
        .value_kind:     global_buffer
      - .address_space:  global
        .offset:         104
        .size:           8
        .value_kind:     global_buffer
      - .address_space:  global
        .offset:         112
        .size:           8
        .value_kind:     global_buffer
    .group_segment_fixed_size: 4384
    .kernarg_segment_align: 8
    .kernarg_segment_size: 120
    .language:       OpenCL C
    .language_version:
      - 2
      - 0
    .max_flat_workgroup_size: 1024
    .name:           _Z8k_bcountPKiS0_S0_PiPjPKfS4_S0_S0_S0_S4_S4_S4_PDF16_S5_
    .private_segment_fixed_size: 0
    .sgpr_count:     26
    .sgpr_spill_count: 0
    .symbol:         _Z8k_bcountPKiS0_S0_PiPjPKfS4_S0_S0_S0_S4_S4_S4_PDF16_S5_.kd
    .uniform_work_group_size: 1
    .uses_dynamic_stack: false
    .vgpr_count:     41
    .vgpr_spill_count: 0
    .wavefront_size: 64
  - .agpr_count:     0
    .args:
      - .actual_access:  read_only
        .address_space:  global
        .offset:         0
        .size:           8
        .value_kind:     global_buffer
      - .actual_access:  read_only
        .address_space:  global
        .offset:         8
        .size:           8
        .value_kind:     global_buffer
      - .actual_access:  read_only
        .address_space:  global
        .offset:         16
        .size:           8
        .value_kind:     global_buffer
      - .actual_access:  read_only
        .address_space:  global
        .offset:         24
        .size:           8
        .value_kind:     global_buffer
      - .actual_access:  write_only
        .address_space:  global
        .offset:         32
        .size:           8
        .value_kind:     global_buffer
      - .actual_access:  write_only
        .address_space:  global
        .offset:         40
        .size:           8
        .value_kind:     global_buffer
      - .actual_access:  read_only
        .address_space:  global
        .offset:         48
        .size:           8
        .value_kind:     global_buffer
      - .actual_access:  read_only
        .address_space:  global
        .offset:         56
        .size:           8
        .value_kind:     global_buffer
      - .actual_access:  read_only
        .address_space:  global
        .offset:         64
        .size:           8
        .value_kind:     global_buffer
      - .actual_access:  read_only
        .address_space:  global
        .offset:         72
        .size:           8
        .value_kind:     global_buffer
      - .actual_access:  read_only
        .address_space:  global
        .offset:         80
        .size:           8
        .value_kind:     global_buffer
      - .actual_access:  read_only
        .address_space:  global
        .offset:         88
        .size:           8
        .value_kind:     global_buffer
      - .actual_access:  read_only
        .address_space:  global
        .offset:         96
        .size:           8
        .value_kind:     global_buffer
      - .actual_access:  read_only
        .address_space:  global
        .offset:         104
        .size:           8
        .value_kind:     global_buffer
      - .address_space:  global
        .offset:         112
        .size:           8
        .value_kind:     global_buffer
      - .address_space:  global
        .offset:         120
        .size:           8
        .value_kind:     global_buffer
      - .offset:         128
        .size:           488
        .value_kind:     by_value
    .group_segment_fixed_size: 145408
    .kernarg_segment_align: 8
    .kernarg_segment_size: 616
    .language:       OpenCL C
    .language_version:
      - 2
      - 0
    .max_flat_workgroup_size: 1024
    .name:           _Z6k_prepPKiS0_S0_S0_PiP15HIP_vector_typeIiLj2EEPKfS6_S0_S0_S0_S6_S6_S6_PDF16_S7_6WSpecs
    .private_segment_fixed_size: 0
    .sgpr_count:     44
    .sgpr_spill_count: 0
    .symbol:         _Z6k_prepPKiS0_S0_S0_PiP15HIP_vector_typeIiLj2EEPKfS6_S0_S0_S0_S6_S6_S6_PDF16_S7_6WSpecs.kd
    .uniform_work_group_size: 1
    .uses_dynamic_stack: false
    .vgpr_count:     128
    .vgpr_spill_count: 0
    .wavefront_size: 64
  - .agpr_count:     0
    .args:
      - .offset:         0
        .size:           104
        .value_kind:     by_value
      - .offset:         104
        .size:           4
        .value_kind:     hidden_block_count_x
      - .offset:         108
        .size:           4
        .value_kind:     hidden_block_count_y
      - .offset:         112
        .size:           4
        .value_kind:     hidden_block_count_z
      - .offset:         116
        .size:           2
        .value_kind:     hidden_group_size_x
      - .offset:         118
        .size:           2
        .value_kind:     hidden_group_size_y
      - .offset:         120
        .size:           2
        .value_kind:     hidden_group_size_z
      - .offset:         122
        .size:           2
        .value_kind:     hidden_remainder_x
      - .offset:         124
        .size:           2
        .value_kind:     hidden_remainder_y
      - .offset:         126
        .size:           2
        .value_kind:     hidden_remainder_z
      - .offset:         144
        .size:           8
        .value_kind:     hidden_global_offset_x
      - .offset:         152
        .size:           8
        .value_kind:     hidden_global_offset_y
      - .offset:         160
        .size:           8
        .value_kind:     hidden_global_offset_z
      - .offset:         168
        .size:           2
        .value_kind:     hidden_grid_dims
    .group_segment_fixed_size: 155140
    .kernarg_segment_align: 8
    .kernarg_segment_size: 360
    .language:       OpenCL C
    .language_version:
      - 2
      - 0
    .max_flat_workgroup_size: 768
    .name:           _Z12k_layer_pool9LayerArgs
    .private_segment_fixed_size: 0
    .sgpr_count:     50
    .sgpr_spill_count: 0
    .symbol:         _Z12k_layer_pool9LayerArgs.kd
    .uniform_work_group_size: 1
    .uses_dynamic_stack: false
    .vgpr_count:     168
    .vgpr_spill_count: 0
    .wavefront_size: 64
  - .agpr_count:     0
    .args:
      - .actual_access:  read_only
        .address_space:  global
        .offset:         0
        .size:           8
        .value_kind:     global_buffer
      - .actual_access:  read_only
        .address_space:  global
        .offset:         8
        .size:           8
        .value_kind:     global_buffer
      - .actual_access:  read_only
        .address_space:  global
        .offset:         16
        .size:           8
        .value_kind:     global_buffer
      - .actual_access:  read_only
        .address_space:  global
        .offset:         24
        .size:           8
        .value_kind:     global_buffer
      - .actual_access:  read_only
        .address_space:  global
        .offset:         32
        .size:           8
        .value_kind:     global_buffer
      - .actual_access:  read_only
        .address_space:  global
        .offset:         40
        .size:           8
        .value_kind:     global_buffer
      - .actual_access:  read_only
        .address_space:  global
        .offset:         48
        .size:           8
        .value_kind:     global_buffer
      - .actual_access:  write_only
        .address_space:  global
        .offset:         56
        .size:           8
        .value_kind:     global_buffer
    .group_segment_fixed_size: 2560
    .kernarg_segment_align: 8
    .kernarg_segment_size: 64
    .language:       OpenCL C
    .language_version:
      - 2
      - 0
    .max_flat_workgroup_size: 512
    .name:           _Z5k_mlpPKjPKfS2_S2_S2_S2_S2_Pf
    .private_segment_fixed_size: 0
    .sgpr_count:     18
    .sgpr_spill_count: 0
    .symbol:         _Z5k_mlpPKjPKfS2_S2_S2_S2_S2_Pf.kd
    .uniform_work_group_size: 1
    .uses_dynamic_stack: false
    .vgpr_count:     120
    .vgpr_spill_count: 0
    .wavefront_size: 64
  - .agpr_count:     0
    .args:
      - .offset:         0
        .size:           104
        .value_kind:     by_value
      - .offset:         104
        .size:           104
        .value_kind:     by_value
      - .offset:         208
        .size:           4
        .value_kind:     by_value
      - .offset:         216
        .size:           4
        .value_kind:     hidden_block_count_x
      - .offset:         220
        .size:           4
        .value_kind:     hidden_block_count_y
      - .offset:         224
        .size:           4
        .value_kind:     hidden_block_count_z
      - .offset:         228
        .size:           2
        .value_kind:     hidden_group_size_x
      - .offset:         230
        .size:           2
        .value_kind:     hidden_group_size_y
      - .offset:         232
        .size:           2
        .value_kind:     hidden_group_size_z
      - .offset:         234
        .size:           2
        .value_kind:     hidden_remainder_x
      - .offset:         236
        .size:           2
        .value_kind:     hidden_remainder_y
      - .offset:         238
        .size:           2
        .value_kind:     hidden_remainder_z
      - .offset:         256
        .size:           8
        .value_kind:     hidden_global_offset_x
      - .offset:         264
        .size:           8
        .value_kind:     hidden_global_offset_y
      - .offset:         272
        .size:           8
        .value_kind:     hidden_global_offset_z
      - .offset:         280
        .size:           2
        .value_kind:     hidden_grid_dims
    .group_segment_fixed_size: 151044
    .kernarg_segment_align: 8
    .kernarg_segment_size: 472
    .language:       OpenCL C
    .language_version:
      - 2
      - 0
    .max_flat_workgroup_size: 768
    .name:           _Z10k_layer_fhILi96ELb1EEv9LayerArgsS0_i
    .private_segment_fixed_size: 0
    .sgpr_count:     52
    .sgpr_spill_count: 0
    .symbol:         _Z10k_layer_fhILi96ELb1EEv9LayerArgsS0_i.kd
    .uniform_work_group_size: 1
    .uses_dynamic_stack: false
    .vgpr_count:     168
    .vgpr_spill_count: 0
    .wavefront_size: 64
  - .agpr_count:     0
    .args:
      - .offset:         0
        .size:           104
        .value_kind:     by_value
      - .offset:         104
        .size:           104
        .value_kind:     by_value
      - .offset:         208
        .size:           4
        .value_kind:     by_value
      - .offset:         216
        .size:           4
        .value_kind:     hidden_block_count_x
      - .offset:         220
        .size:           4
        .value_kind:     hidden_block_count_y
      - .offset:         224
        .size:           4
        .value_kind:     hidden_block_count_z
      - .offset:         228
        .size:           2
        .value_kind:     hidden_group_size_x
      - .offset:         230
        .size:           2
        .value_kind:     hidden_group_size_y
      - .offset:         232
        .size:           2
        .value_kind:     hidden_group_size_z
      - .offset:         234
        .size:           2
        .value_kind:     hidden_remainder_x
      - .offset:         236
        .size:           2
        .value_kind:     hidden_remainder_y
      - .offset:         238
        .size:           2
        .value_kind:     hidden_remainder_z
      - .offset:         256
        .size:           8
        .value_kind:     hidden_global_offset_x
      - .offset:         264
        .size:           8
        .value_kind:     hidden_global_offset_y
      - .offset:         272
        .size:           8
        .value_kind:     hidden_global_offset_z
      - .offset:         280
        .size:           2
        .value_kind:     hidden_grid_dims
    .group_segment_fixed_size: 151044
    .kernarg_segment_align: 8
    .kernarg_segment_size: 472
    .language:       OpenCL C
    .language_version:
      - 2
      - 0
    .max_flat_workgroup_size: 768
    .name:           _Z10k_layer_fhILi128ELb1EEv9LayerArgsS0_i
    .private_segment_fixed_size: 0
    .sgpr_count:     45
    .sgpr_spill_count: 0
    .symbol:         _Z10k_layer_fhILi128ELb1EEv9LayerArgsS0_i.kd
    .uniform_work_group_size: 1
    .uses_dynamic_stack: false
    .vgpr_count:     168
    .vgpr_spill_count: 0
    .wavefront_size: 64
